# speedup vs baseline: 1.0569x; 1.0569x over previous
.LBB4_8:
	s_and_b64 vcc, exec, s[0:1]
	s_cbranch_vccz .LBB4_11
	s_lshl_b32 s0, s2, 10
	s_add_i32 s0, s0, s3
	v_lshrrev_b32_e32 v3, 6, v0
	v_lshlrev_b32_e32 v4, 12, v90
	v_lshl_or_b32 v4, v3, 8, v4
	v_lshl_or_b32 v4, v89, 2, v4
	v_add_u32_e32 v102, 0xe000, v4
	v_lshlrev_b32_e32 v5, 13, v3
	s_mov_b32 s4, 0xe000
	v_add3_u32 v103, v5, v88, s4
	v_mul_u32_u24_e32 v6, 0x186a00, v3
	v_add3_u32 v104, s0, v6, v88
	v_add_u32_e32 v105, 0x30d40, v104
	v_add_u32_e32 v106, 0x61a80, v104
	v_add_u32_e32 v107, 0x927c0, v104
	v_add_u32_e32 v108, 0xc3500, v104
	v_add_u32_e32 v109, 0xf4240, v104
	v_add_u32_e32 v110, 0x124f80, v104
	v_add_u32_e32 v111, 0x155cc0, v104
	s_mov_b32 s0, 0
	s_waitcnt vmcnt(0)
.LBB4_10:
	ds_read_b128 v[16:19], v88
	ds_read_b128 v[90:93], v88 offset:1024
	s_waitcnt lgkmcnt(1)
	v_mfma_f32_32x32x16_f16 v[0:15], v[16:19], v[32:35], 0
	v_mfma_f32_32x32x16_f16 v[16:31], v[16:19], v[40:43], 0
	s_waitcnt lgkmcnt(0)
	v_mfma_f32_32x32x16_f16 v[0:15], v[90:93], v[36:39], v[0:15]
	v_mfma_f32_32x32x16_f16 v[16:31], v[90:93], v[44:47], v[16:31]
	ds_read_b128 v[90:93], v88 offset:2048
	ds_read_b128 v[94:97], v88 offset:3072
	s_waitcnt lgkmcnt(1)
	v_mfma_f32_32x32x16_f16 v[0:15], v[90:93], v[48:51], v[0:15]
	v_mfma_f32_32x32x16_f16 v[16:31], v[90:93], v[56:59], v[16:31]
	s_waitcnt lgkmcnt(0)
	v_mfma_f32_32x32x16_f16 v[0:15], v[94:97], v[52:55], v[0:15]
	v_mfma_f32_32x32x16_f16 v[16:31], v[94:97], v[60:63], v[16:31]
	ds_read_b128 v[90:93], v88 offset:4096
	ds_read_b128 v[94:97], v88 offset:5120
	ds_read_b128 v[98:101], v88 offset:6144
	v_add_u32_e32 v88, 0x1c00, v88
	s_waitcnt lgkmcnt(2)
	v_mfma_f32_32x32x16_f16 v[0:15], v[90:93], v[64:67], v[0:15]
	v_mfma_f32_32x32x16_f16 v[16:31], v[90:93], v[68:71], v[16:31]
	s_waitcnt lgkmcnt(1)
	v_mfma_f32_32x32x16_f16 v[0:15], v[94:97], v[72:75], v[0:15]
	v_mfma_f32_32x32x16_f16 v[16:31], v[94:97], v[76:79], v[16:31]
	s_waitcnt lgkmcnt(0)
	v_mfma_f32_32x32x16_f16 v[0:15], v[98:101], v[80:83], v[0:15]
	v_mfma_f32_32x32x16_f16 v[16:31], v[98:101], v[84:87], v[16:31]
	s_nop 11
	s_barrier
	ds_write_b32 v102, v0 offset:0
	ds_write_b32 v102, v1 offset:1024
	ds_write_b32 v102, v2 offset:2048
	ds_write_b32 v102, v3 offset:3072
	ds_write_b32 v102, v4 offset:8192
	ds_write_b32 v102, v5 offset:9216
	ds_write_b32 v102, v6 offset:10240
	ds_write_b32 v102, v7 offset:11264
	ds_write_b32 v102, v8 offset:16384
	ds_write_b32 v102, v9 offset:17408
	ds_write_b32 v102, v10 offset:18432
	ds_write_b32 v102, v11 offset:19456
	ds_write_b32 v102, v12 offset:24576
	ds_write_b32 v102, v13 offset:25600
	ds_write_b32 v102, v14 offset:26624
	ds_write_b32 v102, v15 offset:27648
	ds_write_b32 v102, v16 offset:128
	ds_write_b32 v102, v17 offset:1152
	ds_write_b32 v102, v18 offset:2176
	ds_write_b32 v102, v19 offset:3200
	ds_write_b32 v102, v20 offset:8320
	ds_write_b32 v102, v21 offset:9344
	ds_write_b32 v102, v22 offset:10368
	ds_write_b32 v102, v23 offset:11392
	ds_write_b32 v102, v24 offset:16512
	ds_write_b32 v102, v25 offset:17536
	ds_write_b32 v102, v26 offset:18560
	ds_write_b32 v102, v27 offset:19584
	ds_write_b32 v102, v28 offset:24704
	ds_write_b32 v102, v29 offset:25728
	ds_write_b32 v102, v30 offset:26752
	ds_write_b32 v102, v31 offset:27776
	s_waitcnt lgkmcnt(0)
	s_barrier
	ds_read_b128 v[0:3], v103 offset:0
	ds_read_b128 v[4:7], v103 offset:1024
	ds_read_b128 v[8:11], v103 offset:2048
	ds_read_b128 v[12:15], v103 offset:3072
	ds_read_b128 v[16:19], v103 offset:4096
	ds_read_b128 v[20:23], v103 offset:5120
	ds_read_b128 v[24:27], v103 offset:6144
	ds_read_b128 v[28:31], v103 offset:7168
	s_waitcnt lgkmcnt(7)
	global_store_dwordx4 v104, v[0:3], s[8:9]
	s_waitcnt lgkmcnt(6)
	global_store_dwordx4 v105, v[4:7], s[8:9]
	s_waitcnt lgkmcnt(5)
	global_store_dwordx4 v106, v[8:11], s[8:9]
	s_waitcnt lgkmcnt(4)
	global_store_dwordx4 v107, v[12:15], s[8:9]
	s_waitcnt lgkmcnt(3)
	global_store_dwordx4 v108, v[16:19], s[8:9]
	s_waitcnt lgkmcnt(2)
	global_store_dwordx4 v109, v[20:23], s[8:9]
	s_waitcnt lgkmcnt(1)
	global_store_dwordx4 v110, v[24:27], s[8:9]
	s_waitcnt lgkmcnt(0)
	global_store_dwordx4 v111, v[28:31], s[8:9]
	s_add_u32 s8, s8, 0x61a800
	s_addc_u32 s9, s9, 0
	s_add_i32 s0, s0, 1
	s_cmp_eq_u32 s0, 8
	s_cbranch_scc0 .LBB4_10

	.amdhsa_kernel _Z9fc_kernelPKDv8_DF16_S1_Pf
		.amdhsa_group_segment_fixed_size 90112
		.amdhsa_private_segment_fixed_size 0
		.amdhsa_kernarg_size 24
		.amdhsa_user_sgpr_count 2
		.amdhsa_user_sgpr_dispatch_ptr 0
		.amdhsa_user_sgpr_queue_ptr 0
		.amdhsa_user_sgpr_kernarg_segment_ptr 1
		.amdhsa_user_sgpr_dispatch_id 0
		.amdhsa_user_sgpr_kernarg_preload_length 0
		.amdhsa_user_sgpr_kernarg_preload_offset 0
		.amdhsa_user_sgpr_private_segment_size 0
		.amdhsa_uses_dynamic_stack 0
		.amdhsa_enable_private_segment 0
		.amdhsa_system_sgpr_workgroup_id_x 1
		.amdhsa_system_sgpr_workgroup_id_y 0
		.amdhsa_system_sgpr_workgroup_id_z 0
		.amdhsa_system_sgpr_workgroup_info 0
		.amdhsa_system_vgpr_workitem_id 0
		.amdhsa_next_free_vgpr 169
		.amdhsa_next_free_sgpr 96
		.amdhsa_accum_offset 128
		.amdhsa_reserve_vcc 1
		.amdhsa_float_round_mode_32 0
		.amdhsa_float_round_mode_16_64 0
		.amdhsa_float_denorm_mode_32 3
		.amdhsa_float_denorm_mode_16_64 3
		.amdhsa_dx10_clamp 1
		.amdhsa_ieee_mode 1
		.amdhsa_fp16_overflow 0
		.amdhsa_tg_split 0
		.amdhsa_exception_fp_ieee_invalid_op 0
		.amdhsa_exception_fp_denorm_src 0
		.amdhsa_exception_fp_ieee_div_zero 0
		.amdhsa_exception_fp_ieee_overflow 0
		.amdhsa_exception_fp_ieee_underflow 0
		.amdhsa_exception_fp_ieee_inexact 0
		.amdhsa_exception_int_div_zero 0
	.end_amdhsa_kernel

amdhsa.kernels:
  - .agpr_count:     0
    .args:
      - .actual_access:  read_only
        .address_space:  global
        .offset:         0
        .size:           8
        .value_kind:     global_buffer
      - .actual_access:  read_only
        .address_space:  global
        .offset:         8
        .size:           8
        .value_kind:     global_buffer
      - .actual_access:  read_only
        .address_space:  global
        .offset:         16
        .size:           8
        .value_kind:     global_buffer
      - .actual_access:  read_only
        .address_space:  global
        .offset:         24
        .size:           8
        .value_kind:     global_buffer
      - .actual_access:  read_only
        .address_space:  global
        .offset:         32
        .size:           8
        .value_kind:     global_buffer
      - .actual_access:  write_only
        .address_space:  global
        .offset:         40
        .size:           8
        .value_kind:     global_buffer
      - .actual_access:  write_only
        .address_space:  global
        .offset:         48
        .size:           8
        .value_kind:     global_buffer
      - .actual_access:  write_only
        .address_space:  global
        .offset:         56
        .size:           8
        .value_kind:     global_buffer
    .group_segment_fixed_size: 0
    .kernarg_segment_align: 8
    .kernarg_segment_size: 64
    .language:       OpenCL C
    .language_version:
      - 2
      - 0
    .max_flat_workgroup_size: 256
    .name:           _Z11prep_kernelPKfS0_S0_S0_S0_PDv8_DF16_S2_Pi
    .private_segment_fixed_size: 0
    .sgpr_count:     26
    .sgpr_spill_count: 0
    .symbol:         _Z11prep_kernelPKfS0_S0_S0_S0_PDv8_DF16_S2_Pi.kd
    .uniform_work_group_size: 1
    .uses_dynamic_stack: false
    .vgpr_count:     18
    .vgpr_spill_count: 0
    .wavefront_size: 64
  - .agpr_count:     0
    .args:
      - .actual_access:  read_only
        .address_space:  global
        .offset:         0
        .size:           8
        .value_kind:     global_buffer
      - .actual_access:  read_only
        .address_space:  global
        .offset:         8
        .size:           8
        .value_kind:     global_buffer
      - .actual_access:  read_only
        .address_space:  global
        .offset:         16
        .size:           8
        .value_kind:     global_buffer
      - .actual_access:  read_only
        .address_space:  global
        .offset:         24
        .size:           8
        .value_kind:     global_buffer
      - .actual_access:  read_only
        .address_space:  global
        .offset:         32
        .size:           8
        .value_kind:     global_buffer
      - .actual_access:  read_only
        .address_space:  global
        .offset:         40
        .size:           8
        .value_kind:     global_buffer
      - .actual_access:  read_only
        .address_space:  global
        .offset:         48
        .size:           8
        .value_kind:     global_buffer
      - .actual_access:  read_only
        .address_space:  global
        .offset:         56
        .size:           8
        .value_kind:     global_buffer
      - .actual_access:  read_only
        .address_space:  global
        .offset:         64
        .size:           8
        .value_kind:     global_buffer
      - .actual_access:  read_only
        .address_space:  global
        .offset:         72
        .size:           8
        .value_kind:     global_buffer
      - .actual_access:  read_only
        .address_space:  global
        .offset:         80
        .size:           8
        .value_kind:     global_buffer
      - .actual_access:  read_only
        .address_space:  global
        .offset:         88
        .size:           8
        .value_kind:     global_buffer
      - .actual_access:  read_only
        .address_space:  global
        .offset:         96
        .size:           8
        .value_kind:     global_buffer
      - .actual_access:  read_only
        .address_space:  global
        .offset:         104
        .size:           8
        .value_kind:     global_buffer
      - .actual_access:  write_only
        .address_space:  global
        .offset:         112
        .size:           8
        .value_kind:     global_buffer
      - .offset:         120
        .size:           4
        .value_kind:     by_value
      - .actual_access:  read_only
        .address_space:  global
        .offset:         128
        .size:           8
        .value_kind:     global_buffer
      - .actual_access:  read_only
        .address_space:  global
        .offset:         136
        .size:           8
        .value_kind:     global_buffer
      - .actual_access:  write_only
        .address_space:  global
        .offset:         144
        .size:           8
        .value_kind:     global_buffer
      - .actual_access:  read_only
        .address_space:  global
        .offset:         152
        .size:           8
        .value_kind:     global_buffer
      - .actual_access:  read_only
        .address_space:  global
        .offset:         160
        .size:           8
        .value_kind:     global_buffer
      - .address_space:  global
        .offset:         168
        .size:           8
        .value_kind:     global_buffer
      - .actual_access:  write_only
        .address_space:  global
        .offset:         176
        .size:           8
        .value_kind:     global_buffer
      - .address_space:  global
        .offset:         184
        .size:           8
        .value_kind:     global_buffer
      - .actual_access:  write_only
        .address_space:  global
        .offset:         192
        .size:           8
        .value_kind:     global_buffer
      - .actual_access:  write_only
        .address_space:  global
        .offset:         200
        .size:           8
        .value_kind:     global_buffer
    .group_segment_fixed_size: 21760
    .kernarg_segment_align: 8
    .kernarg_segment_size: 208
    .language:       OpenCL C
    .language_version:
      - 2
      - 0
    .max_flat_workgroup_size: 256
    .name:           _Z12embed_kernelPKiS0_S0_S0_S0_PKfS2_S2_S2_S2_S2_S2_S2_PKDv8_DF16_PfiS2_S2_PS3_S0_S0_PiS8_S8_P15HIP_vector_typeIiLj2EES8_
    .private_segment_fixed_size: 0
    .sgpr_count:     44
    .sgpr_spill_count: 0
    .symbol:         _Z12embed_kernelPKiS0_S0_S0_S0_PKfS2_S2_S2_S2_S2_S2_S2_PKDv8_DF16_PfiS2_S2_PS3_S0_S0_PiS8_S8_P15HIP_vector_typeIiLj2EES8_.kd
    .uniform_work_group_size: 1
    .uses_dynamic_stack: false
    .vgpr_count:     166
    .vgpr_spill_count: 0
    .wavefront_size: 64
  - .agpr_count:     0
    .args:
      - .actual_access:  read_only
        .address_space:  global
        .offset:         0
        .size:           8
        .value_kind:     global_buffer
      - .actual_access:  read_only
        .address_space:  global
        .offset:         8
        .size:           8
        .value_kind:     global_buffer
      - .actual_access:  read_only
        .address_space:  global
        .offset:         16
        .size:           8
        .value_kind:     global_buffer
      - .actual_access:  read_only
        .address_space:  global
        .offset:         24
        .size:           8
        .value_kind:     global_buffer
      - .actual_access:  read_only
        .address_space:  global
        .offset:         32
        .size:           8
        .value_kind:     global_buffer
      - .actual_access:  read_only
        .address_space:  global
        .offset:         40
        .size:           8
        .value_kind:     global_buffer
      - .actual_access:  read_only
        .address_space:  global
        .offset:         48
        .size:           8
        .value_kind:     global_buffer
      - .actual_access:  read_only
        .address_space:  global
        .offset:         56
        .size:           8
        .value_kind:     global_buffer
      - .actual_access:  write_only
        .address_space:  global
        .offset:         64
        .size:           8
        .value_kind:     global_buffer
      - .offset:         72
        .size:           4
        .value_kind:     by_value
    .group_segment_fixed_size: 30720
    .kernarg_segment_align: 8
    .kernarg_segment_size: 76
    .language:       OpenCL C
    .language_version:
      - 2
      - 0
    .max_flat_workgroup_size: 256
    .name:           _Z10gru_kernelPKfPKiS2_S2_PK15HIP_vector_typeIiLj2EEPKDv8_DF16_S0_S0_Pfi
    .private_segment_fixed_size: 0
    .sgpr_count:     31
    .sgpr_spill_count: 0
    .symbol:         _Z10gru_kernelPKfPKiS2_S2_PK15HIP_vector_typeIiLj2EEPKDv8_DF16_S0_S0_Pfi.kd
    .uniform_work_group_size: 1
    .uses_dynamic_stack: false
    .vgpr_count:     230
    .vgpr_spill_count: 0
    .wavefront_size: 64
  - .agpr_count:     0
    .args:
      - .actual_access:  read_only
        .address_space:  global
        .offset:         0
        .size:           8
        .value_kind:     global_buffer
      - .actual_access:  read_only
        .address_space:  global
        .offset:         8
        .size:           8
        .value_kind:     global_buffer
      - .actual_access:  write_only
        .address_space:  global
        .offset:         16
        .size:           8
        .value_kind:     global_buffer
    .group_segment_fixed_size: 1024
    .kernarg_segment_align: 8
    .kernarg_segment_size: 24
    .language:       OpenCL C
    .language_version:
      - 2
      - 0
    .max_flat_workgroup_size: 256
    .name:           _Z11pool_kernelPKfPKiPDF16_
    .private_segment_fixed_size: 0
    .sgpr_count:     16
    .sgpr_spill_count: 0
    .symbol:         _Z11pool_kernelPKfPKiPDF16_.kd
    .uniform_work_group_size: 1
    .uses_dynamic_stack: false
    .vgpr_count:     18
    .vgpr_spill_count: 0
    .wavefront_size: 64
  - .agpr_count:     0
    .args:
      - .actual_access:  read_only
        .address_space:  global
        .offset:         0
        .size:           8
        .value_kind:     global_buffer
      - .actual_access:  read_only
        .address_space:  global
        .offset:         8
        .size:           8
        .value_kind:     global_buffer
      - .actual_access:  write_only
        .address_space:  global
        .offset:         16
        .size:           8
        .value_kind:     global_buffer
    .group_segment_fixed_size: 90112
    .kernarg_segment_align: 8
    .kernarg_segment_size: 24
    .language:       OpenCL C
    .language_version:
      - 2
      - 0
    .max_flat_workgroup_size: 256
    .name:           _Z9fc_kernelPKDv8_DF16_S1_Pf
    .private_segment_fixed_size: 0
    .sgpr_count:     17
    .sgpr_spill_count: 0
    .symbol:         _Z9fc_kernelPKDv8_DF16_S1_Pf.kd
    .uniform_work_group_size: 1
    .uses_dynamic_stack: false
    .vgpr_count:     126
    .vgpr_spill_count: 0
    .wavefront_size: 64
